# gdnprep stage D: diagonal-block forward substitution with the T column in registers (unrolled, broadcast L rows double buffered) instead of LDS-resident loops
# speedup vs baseline: 1.0213x; 1.0213x over previous
; DI void gdn_prep_unit(const Params& p, int U, char* lds) {
;     ...
;     if (wid < 2 && lane < 32) {
;       const int o = 32 * wid;
;       for (int i = 0; i < 32; ++i) {
;         float a0 = (lane == i) ? 1.f : 0.f, a1 = 0.f, a2 = 0.f, a3 = 0.f;
;         const float* Li = Lm + (o + i) * 68 + o;
;         int j = 0;
; #pragma unroll 4
;         for (; j + 4 <= i; j += 4) {
;           const f32x4 Lv = *(const f32x4*)(Li + j);
;           a0 -= Lv[0] * Ts[(o + j) * 64 + o + lane]; a1 -= Lv[1] * Ts[(o + j + 1) * 64 + o + lane]; a2 -= Lv[2] * Ts[(o + j + 2) * 64 + o + lane]; a3 -= Lv[3] * Ts[(o + j + 3) * 64 + o + lane];
;         }
;         for (; j < i; ++j) a0 -= Li[j] * Ts[(o + j) * 64 + o + lane];
;         Ts[(o + i) * 64 + o + lane] = (a0 + a1) + (a2 + a3);
.LBB0_1103:
	s_or_b64 exec, exec, s[0:1]
	v_cmp_gt_i32_e64 s[0:1], 2, v181
	v_cmp_gt_u32_e32 vcc, 32, v178
	v_lshlrev_b32_e32 v12, 3, v31
	s_and_b64 s[10:11], s[0:1], vcc
	v_lshlrev_b32_e32 v10, 2, v178
	s_waitcnt lgkmcnt(0)
	s_barrier
	s_and_saveexec_b64 s[8:9], s[10:11]
	s_cbranch_execz .LBB0_1119
	s_movk_i32 s10, 0x2280
	v_mul_lo_u32 v240, v181, s10
	s_mov_b32 s11, 0xcc00
	v_add3_u32 v240, v240, v146, s11
	s_movk_i32 s10, 0x2080
	v_mul_lo_u32 v241, v181, s10
	v_add3_u32 v241, v241, v146, v10
	v_cmp_eq_u32_e32 vcc, 0, v178
	s_nop 1
	v_cndmask_b32_e64 v0, 0, 1.0, vcc
	ds_write_b32 v241, v0
	ds_read_b128 v[56:59], v240 offset:272
	ds_read_b128 v[220:223], v240 offset:544
	v_cmp_eq_u32_e32 vcc, 1, v178
	v_mov_b32_e32 v237, 0
	v_mov_b32_e32 v238, 0
	v_mov_b32_e32 v239, 0
	v_cndmask_b32_e64 v236, 0, 1.0, vcc
	s_waitcnt lgkmcnt(1)
	v_fma_f32 v236, -v56, v0, v236
	v_add_f32_e32 v236, v236, v237
	v_add_f32_e32 v238, v238, v239
	v_add_f32_e32 v1, v236, v238
	ds_write_b32 v241, v1 offset:256
	ds_read_b128 v[56:59], v240 offset:816
	v_cmp_eq_u32_e32 vcc, 2, v178
	v_mov_b32_e32 v237, 0
	v_mov_b32_e32 v238, 0
	v_mov_b32_e32 v239, 0
	v_cndmask_b32_e64 v236, 0, 1.0, vcc
	s_waitcnt lgkmcnt(2)
	v_fma_f32 v236, -v220, v0, v236
	v_fma_f32 v237, -v221, v1, v237
	v_add_f32_e32 v236, v236, v237
	v_add_f32_e32 v238, v238, v239
	v_add_f32_e32 v2, v236, v238
	ds_write_b32 v241, v2 offset:512
	ds_read_b128 v[220:223], v240 offset:1088
	v_cmp_eq_u32_e32 vcc, 3, v178
	v_mov_b32_e32 v237, 0
	v_mov_b32_e32 v238, 0
	v_mov_b32_e32 v239, 0
	v_cndmask_b32_e64 v236, 0, 1.0, vcc
	s_waitcnt lgkmcnt(2)
	v_fma_f32 v236, -v56, v0, v236
	v_fma_f32 v237, -v57, v1, v237
	v_fma_f32 v238, -v58, v2, v238
	v_add_f32_e32 v236, v236, v237
	v_add_f32_e32 v238, v238, v239
	v_add_f32_e32 v3, v236, v238
	ds_write_b32 v241, v3 offset:768
	ds_read_b128 v[56:59], v240 offset:1360
	ds_read_b128 v[60:63], v240 offset:1376
	v_cmp_eq_u32_e32 vcc, 4, v178
	v_mov_b32_e32 v237, 0
	v_mov_b32_e32 v238, 0
	v_mov_b32_e32 v239, 0
	v_cndmask_b32_e64 v236, 0, 1.0, vcc
	s_waitcnt lgkmcnt(3)
	v_fma_f32 v236, -v220, v0, v236
	v_fma_f32 v237, -v221, v1, v237
	v_fma_f32 v238, -v222, v2, v238
	v_fma_f32 v239, -v223, v3, v239
	v_add_f32_e32 v236, v236, v237
	v_add_f32_e32 v238, v238, v239
	v_add_f32_e32 v4, v236, v238
	ds_write_b32 v241, v4 offset:1024
	ds_read_b128 v[220:223], v240 offset:1632
	ds_read_b128 v[224:227], v240 offset:1648
	v_cmp_eq_u32_e32 vcc, 5, v178
	v_mov_b32_e32 v237, 0
	v_mov_b32_e32 v238, 0
	v_mov_b32_e32 v239, 0
	v_cndmask_b32_e64 v236, 0, 1.0, vcc
	s_waitcnt lgkmcnt(3)
	v_fma_f32 v236, -v56, v0, v236
	v_fma_f32 v237, -v57, v1, v237
	v_fma_f32 v238, -v58, v2, v238
	v_fma_f32 v239, -v59, v3, v239
	v_fma_f32 v236, -v60, v4, v236
	v_add_f32_e32 v236, v236, v237
	v_add_f32_e32 v238, v238, v239
	v_add_f32_e32 v5, v236, v238
	ds_write_b32 v241, v5 offset:1280
	ds_read_b128 v[56:59], v240 offset:1904
	ds_read_b128 v[60:63], v240 offset:1920
	v_cmp_eq_u32_e32 vcc, 6, v178
	v_mov_b32_e32 v237, 0
	v_mov_b32_e32 v238, 0
	v_mov_b32_e32 v239, 0
	v_cndmask_b32_e64 v236, 0, 1.0, vcc
	s_waitcnt lgkmcnt(3)
	v_fma_f32 v236, -v220, v0, v236
	v_fma_f32 v237, -v221, v1, v237
	v_fma_f32 v238, -v222, v2, v238
	v_fma_f32 v239, -v223, v3, v239
	v_fma_f32 v236, -v224, v4, v236
	v_fma_f32 v237, -v225, v5, v237
	v_add_f32_e32 v236, v236, v237
	v_add_f32_e32 v238, v238, v239
	v_add_f32_e32 v6, v236, v238
	ds_write_b32 v241, v6 offset:1536
	ds_read_b128 v[220:223], v240 offset:2176
	ds_read_b128 v[224:227], v240 offset:2192
	v_cmp_eq_u32_e32 vcc, 7, v178
	v_mov_b32_e32 v237, 0
	v_mov_b32_e32 v238, 0
	v_mov_b32_e32 v239, 0
	v_cndmask_b32_e64 v236, 0, 1.0, vcc
	s_waitcnt lgkmcnt(3)
	v_fma_f32 v236, -v56, v0, v236
	v_fma_f32 v237, -v57, v1, v237
	v_fma_f32 v238, -v58, v2, v238
	v_fma_f32 v239, -v59, v3, v239
	v_fma_f32 v236, -v60, v4, v236
	v_fma_f32 v237, -v61, v5, v237
	v_fma_f32 v238, -v62, v6, v238
	v_add_f32_e32 v236, v236, v237
	v_add_f32_e32 v238, v238, v239
	v_add_f32_e32 v7, v236, v238
	ds_write_b32 v241, v7 offset:1792
	ds_read_b128 v[56:59], v240 offset:2448
	ds_read_b128 v[60:63], v240 offset:2464
	ds_read_b128 v[64:67], v240 offset:2480
	v_cmp_eq_u32_e32 vcc, 8, v178
	v_mov_b32_e32 v237, 0
	v_mov_b32_e32 v238, 0
	v_mov_b32_e32 v239, 0
	v_cndmask_b32_e64 v236, 0, 1.0, vcc
	s_waitcnt lgkmcnt(4)
	v_fma_f32 v236, -v220, v0, v236
	v_fma_f32 v237, -v221, v1, v237
	v_fma_f32 v238, -v222, v2, v238
	v_fma_f32 v239, -v223, v3, v239
	v_fma_f32 v236, -v224, v4, v236
	v_fma_f32 v237, -v225, v5, v237
	v_fma_f32 v238, -v226, v6, v238
	v_fma_f32 v239, -v227, v7, v239
	v_add_f32_e32 v236, v236, v237
	v_add_f32_e32 v238, v238, v239
	v_add_f32_e32 v8, v236, v238
	ds_write_b32 v241, v8 offset:2048
	ds_read_b128 v[220:223], v240 offset:2720
	ds_read_b128 v[224:227], v240 offset:2736
	ds_read_b128 v[228:231], v240 offset:2752
	v_cmp_eq_u32_e32 vcc, 9, v178
	v_mov_b32_e32 v237, 0
	v_mov_b32_e32 v238, 0
	v_mov_b32_e32 v239, 0
	v_cndmask_b32_e64 v236, 0, 1.0, vcc
	s_waitcnt lgkmcnt(4)
	v_fma_f32 v236, -v56, v0, v236
	v_fma_f32 v237, -v57, v1, v237
	v_fma_f32 v238, -v58, v2, v238
	v_fma_f32 v239, -v59, v3, v239
	v_fma_f32 v236, -v60, v4, v236
	v_fma_f32 v237, -v61, v5, v237
	v_fma_f32 v238, -v62, v6, v238
	v_fma_f32 v239, -v63, v7, v239
	v_fma_f32 v236, -v64, v8, v236
	v_add_f32_e32 v236, v236, v237
	v_add_f32_e32 v238, v238, v239
	v_add_f32_e32 v9, v236, v238
	ds_write_b32 v241, v9 offset:2304
	ds_read_b128 v[56:59], v240 offset:2992
	ds_read_b128 v[60:63], v240 offset:3008
	ds_read_b128 v[64:67], v240 offset:3024
	v_cmp_eq_u32_e32 vcc, 10, v178
	v_mov_b32_e32 v237, 0
	v_mov_b32_e32 v238, 0
	v_mov_b32_e32 v239, 0
	v_cndmask_b32_e64 v236, 0, 1.0, vcc
	s_waitcnt lgkmcnt(4)
; DI void gdn_prep_unit(const Params& p, int U, char* lds) {
;     ...
;     if (wid < 2 && lane < 32) {
;       const int o = 32 * wid;
;       for (int i = 0; i < 32; ++i) {
;         float a0 = (lane == i) ? 1.f : 0.f, a1 = 0.f, a2 = 0.f, a3 = 0.f;
;         const float* Li = Lm + (o + i) * 68 + o;
;         int j = 0;
; #pragma unroll 4
;         for (; j + 4 <= i; j += 4) {
;           const f32x4 Lv = *(const f32x4*)(Li + j);
;           a0 -= Lv[0] * Ts[(o + j) * 64 + o + lane]; a1 -= Lv[1] * Ts[(o + j + 1) * 64 + o + lane]; a2 -= Lv[2] * Ts[(o + j + 2) * 64 + o + lane]; a3 -= Lv[3] * Ts[(o + j + 3) * 64 + o + lane];
;         }
;         for (; j < i; ++j) a0 -= Li[j] * Ts[(o + j) * 64 + o + lane];
;         Ts[(o + i) * 64 + o + lane] = (a0 + a1) + (a2 + a3);
	v_fma_f32 v236, -v220, v0, v236
	v_fma_f32 v237, -v221, v1, v237
	v_fma_f32 v238, -v222, v2, v238
	v_fma_f32 v239, -v223, v3, v239
	v_fma_f32 v236, -v224, v4, v236
	v_fma_f32 v237, -v225, v5, v237
	v_fma_f32 v238, -v226, v6, v238
	v_fma_f32 v239, -v227, v7, v239
	v_fma_f32 v236, -v228, v8, v236
	v_fma_f32 v237, -v229, v9, v237
	v_add_f32_e32 v236, v236, v237
	v_add_f32_e32 v238, v238, v239
	v_add_f32_e32 v13, v236, v238
	ds_write_b32 v241, v13 offset:2560
	ds_read_b128 v[220:223], v240 offset:3264
	ds_read_b128 v[224:227], v240 offset:3280
	ds_read_b128 v[228:231], v240 offset:3296
	v_cmp_eq_u32_e32 vcc, 11, v178
	v_mov_b32_e32 v237, 0
	v_mov_b32_e32 v238, 0
	v_mov_b32_e32 v239, 0
	v_cndmask_b32_e64 v236, 0, 1.0, vcc
	s_waitcnt lgkmcnt(4)
	v_fma_f32 v236, -v56, v0, v236
	v_fma_f32 v237, -v57, v1, v237
	v_fma_f32 v238, -v58, v2, v238
	v_fma_f32 v239, -v59, v3, v239
	v_fma_f32 v236, -v60, v4, v236
	v_fma_f32 v237, -v61, v5, v237
	v_fma_f32 v238, -v62, v6, v238
	v_fma_f32 v239, -v63, v7, v239
	v_fma_f32 v236, -v64, v8, v236
	v_fma_f32 v237, -v65, v9, v237
	v_fma_f32 v238, -v66, v13, v238
	v_add_f32_e32 v236, v236, v237
	v_add_f32_e32 v238, v238, v239
	v_add_f32_e32 v14, v236, v238
	ds_write_b32 v241, v14 offset:2816
	ds_read_b128 v[56:59], v240 offset:3536
	ds_read_b128 v[60:63], v240 offset:3552
	ds_read_b128 v[64:67], v240 offset:3568
	ds_read_b128 v[68:71], v240 offset:3584
	v_cmp_eq_u32_e32 vcc, 12, v178
	v_mov_b32_e32 v237, 0
	v_mov_b32_e32 v238, 0
	v_mov_b32_e32 v239, 0
	v_cndmask_b32_e64 v236, 0, 1.0, vcc
	s_waitcnt lgkmcnt(5)
	v_fma_f32 v236, -v220, v0, v236
	v_fma_f32 v237, -v221, v1, v237
	v_fma_f32 v238, -v222, v2, v238
	v_fma_f32 v239, -v223, v3, v239
	v_fma_f32 v236, -v224, v4, v236
	v_fma_f32 v237, -v225, v5, v237
	v_fma_f32 v238, -v226, v6, v238
	v_fma_f32 v239, -v227, v7, v239
	v_fma_f32 v236, -v228, v8, v236
	v_fma_f32 v237, -v229, v9, v237
	v_fma_f32 v238, -v230, v13, v238
	v_fma_f32 v239, -v231, v14, v239
	v_add_f32_e32 v236, v236, v237
	v_add_f32_e32 v238, v238, v239
	v_add_f32_e32 v15, v236, v238
	ds_write_b32 v241, v15 offset:3072
	ds_read_b128 v[220:223], v240 offset:3808
	ds_read_b128 v[224:227], v240 offset:3824
	ds_read_b128 v[228:231], v240 offset:3840
	ds_read_b128 v[232:235], v240 offset:3856
	v_cmp_eq_u32_e32 vcc, 13, v178
	v_mov_b32_e32 v237, 0
	v_mov_b32_e32 v238, 0
	v_mov_b32_e32 v239, 0
	v_cndmask_b32_e64 v236, 0, 1.0, vcc
	s_waitcnt lgkmcnt(5)
	v_fma_f32 v236, -v56, v0, v236
	v_fma_f32 v237, -v57, v1, v237
	v_fma_f32 v238, -v58, v2, v238
	v_fma_f32 v239, -v59, v3, v239
	v_fma_f32 v236, -v60, v4, v236
	v_fma_f32 v237, -v61, v5, v237
	v_fma_f32 v238, -v62, v6, v238
	v_fma_f32 v239, -v63, v7, v239
	v_fma_f32 v236, -v64, v8, v236
	v_fma_f32 v237, -v65, v9, v237
	v_fma_f32 v238, -v66, v13, v238
	v_fma_f32 v239, -v67, v14, v239
	v_fma_f32 v236, -v68, v15, v236
	v_add_f32_e32 v236, v236, v237
	v_add_f32_e32 v238, v238, v239
	v_add_f32_e32 v16, v236, v238
	ds_write_b32 v241, v16 offset:3328
	ds_read_b128 v[56:59], v240 offset:4080
	ds_read_b128 v[60:63], v240 offset:4096
	ds_read_b128 v[64:67], v240 offset:4112
	ds_read_b128 v[68:71], v240 offset:4128
	v_cmp_eq_u32_e32 vcc, 14, v178
	v_mov_b32_e32 v237, 0
	v_mov_b32_e32 v238, 0
	v_mov_b32_e32 v239, 0
	v_cndmask_b32_e64 v236, 0, 1.0, vcc
	s_waitcnt lgkmcnt(5)
	v_fma_f32 v236, -v220, v0, v236
	v_fma_f32 v237, -v221, v1, v237
	v_fma_f32 v238, -v222, v2, v238
	v_fma_f32 v239, -v223, v3, v239
	v_fma_f32 v236, -v224, v4, v236
	v_fma_f32 v237, -v225, v5, v237
	v_fma_f32 v238, -v226, v6, v238
	v_fma_f32 v239, -v227, v7, v239
	v_fma_f32 v236, -v228, v8, v236
	v_fma_f32 v237, -v229, v9, v237
	v_fma_f32 v238, -v230, v13, v238
	v_fma_f32 v239, -v231, v14, v239
	v_fma_f32 v236, -v232, v15, v236
	v_fma_f32 v237, -v233, v16, v237
	v_add_f32_e32 v236, v236, v237
	v_add_f32_e32 v238, v238, v239
	v_add_f32_e32 v17, v236, v238
	ds_write_b32 v241, v17 offset:3584
	ds_read_b128 v[220:223], v240 offset:4352
	ds_read_b128 v[224:227], v240 offset:4368
	ds_read_b128 v[228:231], v240 offset:4384
	ds_read_b128 v[232:235], v240 offset:4400
	v_cmp_eq_u32_e32 vcc, 15, v178
	v_mov_b32_e32 v237, 0
	v_mov_b32_e32 v238, 0
	v_mov_b32_e32 v239, 0
	v_cndmask_b32_e64 v236, 0, 1.0, vcc
	s_waitcnt lgkmcnt(5)
	v_fma_f32 v236, -v56, v0, v236
	v_fma_f32 v237, -v57, v1, v237
	v_fma_f32 v238, -v58, v2, v238
	v_fma_f32 v239, -v59, v3, v239
	v_fma_f32 v236, -v60, v4, v236
	v_fma_f32 v237, -v61, v5, v237
	v_fma_f32 v238, -v62, v6, v238
	v_fma_f32 v239, -v63, v7, v239
	v_fma_f32 v236, -v64, v8, v236
	v_fma_f32 v237, -v65, v9, v237
	v_fma_f32 v238, -v66, v13, v238
	v_fma_f32 v239, -v67, v14, v239
	v_fma_f32 v236, -v68, v15, v236
	v_fma_f32 v237, -v69, v16, v237
	v_fma_f32 v238, -v70, v17, v238
	v_add_f32_e32 v236, v236, v237
	v_add_f32_e32 v238, v238, v239
	v_add_f32_e32 v18, v236, v238
	ds_write_b32 v241, v18 offset:3840
	ds_read_b128 v[56:59], v240 offset:4624
	ds_read_b128 v[60:63], v240 offset:4640
	ds_read_b128 v[64:67], v240 offset:4656
	ds_read_b128 v[68:71], v240 offset:4672
	v_cmp_eq_u32_e32 vcc, 16, v178
	v_mov_b32_e32 v237, 0
	v_mov_b32_e32 v238, 0
	v_mov_b32_e32 v239, 0
	v_cndmask_b32_e64 v236, 0, 1.0, vcc
	s_waitcnt lgkmcnt(5)
	v_fma_f32 v236, -v220, v0, v236
	v_fma_f32 v237, -v221, v1, v237
	v_fma_f32 v238, -v222, v2, v238
	v_fma_f32 v239, -v223, v3, v239
	v_fma_f32 v236, -v224, v4, v236
	v_fma_f32 v237, -v225, v5, v237
	v_fma_f32 v238, -v226, v6, v238
	v_fma_f32 v239, -v227, v7, v239
	v_fma_f32 v236, -v228, v8, v236
	v_fma_f32 v237, -v229, v9, v237
	v_fma_f32 v238, -v230, v13, v238
	v_fma_f32 v239, -v231, v14, v239
	v_fma_f32 v236, -v232, v15, v236
	v_fma_f32 v237, -v233, v16, v237
	v_fma_f32 v238, -v234, v17, v238
	v_fma_f32 v239, -v235, v18, v239
	v_add_f32_e32 v236, v236, v237
	v_add_f32_e32 v238, v238, v239
	v_add_f32_e32 v19, v236, v238
	ds_write_b32 v241, v19 offset:4096
	ds_read_b128 v[220:223], v240 offset:4688
	v_cmp_eq_u32_e32 vcc, 17, v178
	v_mov_b32_e32 v237, 0
	v_mov_b32_e32 v238, 0
	v_mov_b32_e32 v239, 0
	v_cndmask_b32_e64 v236, 0, 1.0, vcc
	s_waitcnt lgkmcnt(2)
; DI void gdn_prep_unit(const Params& p, int U, char* lds) {
;     ...
;     if (wid < 2 && lane < 32) {
;       const int o = 32 * wid;
;       for (int i = 0; i < 32; ++i) {
;         float a0 = (lane == i) ? 1.f : 0.f, a1 = 0.f, a2 = 0.f, a3 = 0.f;
;         const float* Li = Lm + (o + i) * 68 + o;
;         int j = 0;
; #pragma unroll 4
;         for (; j + 4 <= i; j += 4) {
;           const f32x4 Lv = *(const f32x4*)(Li + j);
;           a0 -= Lv[0] * Ts[(o + j) * 64 + o + lane]; a1 -= Lv[1] * Ts[(o + j + 1) * 64 + o + lane]; a2 -= Lv[2] * Ts[(o + j + 2) * 64 + o + lane]; a3 -= Lv[3] * Ts[(o + j + 3) * 64 + o + lane];
;         }
;         for (; j < i; ++j) a0 -= Li[j] * Ts[(o + j) * 64 + o + lane];
;         Ts[(o + i) * 64 + o + lane] = (a0 + a1) + (a2 + a3);
	v_fma_f32 v236, -v56, v0, v236
	v_fma_f32 v237, -v57, v1, v237
	v_fma_f32 v238, -v58, v2, v238
	v_fma_f32 v239, -v59, v3, v239
	v_fma_f32 v236, -v60, v4, v236
	v_fma_f32 v237, -v61, v5, v237
	v_fma_f32 v238, -v62, v6, v238
	v_fma_f32 v239, -v63, v7, v239
	v_fma_f32 v236, -v64, v8, v236
	v_fma_f32 v237, -v65, v9, v237
	v_fma_f32 v238, -v66, v13, v238
	v_fma_f32 v239, -v67, v14, v239
	v_fma_f32 v236, -v68, v15, v236
	v_fma_f32 v237, -v69, v16, v237
	v_fma_f32 v238, -v70, v17, v238
	v_fma_f32 v239, -v71, v18, v239
	ds_read_b128 v[56:59], v240 offset:4896
	ds_read_b128 v[60:63], v240 offset:4912
	ds_read_b128 v[64:67], v240 offset:4928
	ds_read_b128 v[68:71], v240 offset:4944
	s_waitcnt lgkmcnt(4)
	v_fma_f32 v236, -v220, v19, v236
	v_add_f32_e32 v236, v236, v237
	v_add_f32_e32 v238, v238, v239
	v_add_f32_e32 v20, v236, v238
	ds_write_b32 v241, v20 offset:4352
	ds_read_b128 v[220:223], v240 offset:4960
	v_cmp_eq_u32_e32 vcc, 18, v178
	v_mov_b32_e32 v237, 0
	v_mov_b32_e32 v238, 0
	v_mov_b32_e32 v239, 0
	v_cndmask_b32_e64 v236, 0, 1.0, vcc
	s_waitcnt lgkmcnt(2)
	v_fma_f32 v236, -v56, v0, v236
	v_fma_f32 v237, -v57, v1, v237
	v_fma_f32 v238, -v58, v2, v238
	v_fma_f32 v239, -v59, v3, v239
	v_fma_f32 v236, -v60, v4, v236
	v_fma_f32 v237, -v61, v5, v237
	v_fma_f32 v238, -v62, v6, v238
	v_fma_f32 v239, -v63, v7, v239
	v_fma_f32 v236, -v64, v8, v236
	v_fma_f32 v237, -v65, v9, v237
	v_fma_f32 v238, -v66, v13, v238
	v_fma_f32 v239, -v67, v14, v239
	v_fma_f32 v236, -v68, v15, v236
	v_fma_f32 v237, -v69, v16, v237
	v_fma_f32 v238, -v70, v17, v238
	v_fma_f32 v239, -v71, v18, v239
	ds_read_b128 v[56:59], v240 offset:5168
	ds_read_b128 v[60:63], v240 offset:5184
	ds_read_b128 v[64:67], v240 offset:5200
	ds_read_b128 v[68:71], v240 offset:5216
	s_waitcnt lgkmcnt(4)
	v_fma_f32 v236, -v220, v19, v236
	v_fma_f32 v237, -v221, v20, v237
	v_add_f32_e32 v236, v236, v237
	v_add_f32_e32 v238, v238, v239
	v_add_f32_e32 v21, v236, v238
	ds_write_b32 v241, v21 offset:4608
	ds_read_b128 v[220:223], v240 offset:5232
	v_cmp_eq_u32_e32 vcc, 19, v178
	v_mov_b32_e32 v237, 0
	v_mov_b32_e32 v238, 0
	v_mov_b32_e32 v239, 0
	v_cndmask_b32_e64 v236, 0, 1.0, vcc
	s_waitcnt lgkmcnt(2)
	v_fma_f32 v236, -v56, v0, v236
	v_fma_f32 v237, -v57, v1, v237
	v_fma_f32 v238, -v58, v2, v238
	v_fma_f32 v239, -v59, v3, v239
	v_fma_f32 v236, -v60, v4, v236
	v_fma_f32 v237, -v61, v5, v237
	v_fma_f32 v238, -v62, v6, v238
	v_fma_f32 v239, -v63, v7, v239
	v_fma_f32 v236, -v64, v8, v236
	v_fma_f32 v237, -v65, v9, v237
	v_fma_f32 v238, -v66, v13, v238
	v_fma_f32 v239, -v67, v14, v239
	v_fma_f32 v236, -v68, v15, v236
	v_fma_f32 v237, -v69, v16, v237
	v_fma_f32 v238, -v70, v17, v238
	v_fma_f32 v239, -v71, v18, v239
	ds_read_b128 v[56:59], v240 offset:5440
	ds_read_b128 v[60:63], v240 offset:5456
	ds_read_b128 v[64:67], v240 offset:5472
	ds_read_b128 v[68:71], v240 offset:5488
	s_waitcnt lgkmcnt(4)
	v_fma_f32 v236, -v220, v19, v236
	v_fma_f32 v237, -v221, v20, v237
	v_fma_f32 v238, -v222, v21, v238
	v_add_f32_e32 v236, v236, v237
	v_add_f32_e32 v238, v238, v239
	v_add_f32_e32 v22, v236, v238
	ds_write_b32 v241, v22 offset:4864
	ds_read_b128 v[220:223], v240 offset:5504
	v_cmp_eq_u32_e32 vcc, 20, v178
	v_mov_b32_e32 v237, 0
	v_mov_b32_e32 v238, 0
	v_mov_b32_e32 v239, 0
	v_cndmask_b32_e64 v236, 0, 1.0, vcc
	s_waitcnt lgkmcnt(2)
	v_fma_f32 v236, -v56, v0, v236
	v_fma_f32 v237, -v57, v1, v237
	v_fma_f32 v238, -v58, v2, v238
	v_fma_f32 v239, -v59, v3, v239
	v_fma_f32 v236, -v60, v4, v236
	v_fma_f32 v237, -v61, v5, v237
	v_fma_f32 v238, -v62, v6, v238
	v_fma_f32 v239, -v63, v7, v239
	v_fma_f32 v236, -v64, v8, v236
	v_fma_f32 v237, -v65, v9, v237
	v_fma_f32 v238, -v66, v13, v238
	v_fma_f32 v239, -v67, v14, v239
	v_fma_f32 v236, -v68, v15, v236
	v_fma_f32 v237, -v69, v16, v237
	v_fma_f32 v238, -v70, v17, v238
	v_fma_f32 v239, -v71, v18, v239
	ds_read_b128 v[56:59], v240 offset:5712
	ds_read_b128 v[60:63], v240 offset:5728
	ds_read_b128 v[64:67], v240 offset:5744
	ds_read_b128 v[68:71], v240 offset:5760
	s_waitcnt lgkmcnt(4)
	v_fma_f32 v236, -v220, v19, v236
	v_fma_f32 v237, -v221, v20, v237
	v_fma_f32 v238, -v222, v21, v238
	v_fma_f32 v239, -v223, v22, v239
	v_add_f32_e32 v236, v236, v237
	v_add_f32_e32 v238, v238, v239
	v_add_f32_e32 v23, v236, v238
	ds_write_b32 v241, v23 offset:5120
	ds_read_b128 v[220:223], v240 offset:5776
	ds_read_b128 v[224:227], v240 offset:5792
	v_cmp_eq_u32_e32 vcc, 21, v178
	v_mov_b32_e32 v237, 0
	v_mov_b32_e32 v238, 0
	v_mov_b32_e32 v239, 0
	v_cndmask_b32_e64 v236, 0, 1.0, vcc
	s_waitcnt lgkmcnt(3)
	v_fma_f32 v236, -v56, v0, v236
	v_fma_f32 v237, -v57, v1, v237
	v_fma_f32 v238, -v58, v2, v238
	v_fma_f32 v239, -v59, v3, v239
	v_fma_f32 v236, -v60, v4, v236
	v_fma_f32 v237, -v61, v5, v237
	v_fma_f32 v238, -v62, v6, v238
	v_fma_f32 v239, -v63, v7, v239
	v_fma_f32 v236, -v64, v8, v236
	v_fma_f32 v237, -v65, v9, v237
	v_fma_f32 v238, -v66, v13, v238
	v_fma_f32 v239, -v67, v14, v239
	v_fma_f32 v236, -v68, v15, v236
	v_fma_f32 v237, -v69, v16, v237
	v_fma_f32 v238, -v70, v17, v238
	v_fma_f32 v239, -v71, v18, v239
	ds_read_b128 v[56:59], v240 offset:5984
	ds_read_b128 v[60:63], v240 offset:6000
	ds_read_b128 v[64:67], v240 offset:6016
	ds_read_b128 v[68:71], v240 offset:6032
	s_waitcnt lgkmcnt(4)
	v_fma_f32 v236, -v220, v19, v236
	v_fma_f32 v237, -v221, v20, v237
	v_fma_f32 v238, -v222, v21, v238
	v_fma_f32 v239, -v223, v22, v239
	v_fma_f32 v236, -v224, v23, v236
	v_add_f32_e32 v236, v236, v237
	v_add_f32_e32 v238, v238, v239
	v_add_f32_e32 v24, v236, v238
	ds_write_b32 v241, v24 offset:5376
	ds_read_b128 v[220:223], v240 offset:6048
	ds_read_b128 v[224:227], v240 offset:6064
	v_cmp_eq_u32_e32 vcc, 22, v178
	v_mov_b32_e32 v237, 0
	v_mov_b32_e32 v238, 0
	v_mov_b32_e32 v239, 0
	v_cndmask_b32_e64 v236, 0, 1.0, vcc
	s_waitcnt lgkmcnt(3)
; DI void gdn_prep_unit(const Params& p, int U, char* lds) {
;     ...
;     if (wid < 2 && lane < 32) {
;       const int o = 32 * wid;
;       for (int i = 0; i < 32; ++i) {
;         float a0 = (lane == i) ? 1.f : 0.f, a1 = 0.f, a2 = 0.f, a3 = 0.f;
;         const float* Li = Lm + (o + i) * 68 + o;
;         int j = 0;
; #pragma unroll 4
;         for (; j + 4 <= i; j += 4) {
;           const f32x4 Lv = *(const f32x4*)(Li + j);
;           a0 -= Lv[0] * Ts[(o + j) * 64 + o + lane]; a1 -= Lv[1] * Ts[(o + j + 1) * 64 + o + lane]; a2 -= Lv[2] * Ts[(o + j + 2) * 64 + o + lane]; a3 -= Lv[3] * Ts[(o + j + 3) * 64 + o + lane];
;         }
;         for (; j < i; ++j) a0 -= Li[j] * Ts[(o + j) * 64 + o + lane];
;         Ts[(o + i) * 64 + o + lane] = (a0 + a1) + (a2 + a3);
	v_fma_f32 v236, -v56, v0, v236
	v_fma_f32 v237, -v57, v1, v237
	v_fma_f32 v238, -v58, v2, v238
	v_fma_f32 v239, -v59, v3, v239
	v_fma_f32 v236, -v60, v4, v236
	v_fma_f32 v237, -v61, v5, v237
	v_fma_f32 v238, -v62, v6, v238
	v_fma_f32 v239, -v63, v7, v239
	v_fma_f32 v236, -v64, v8, v236
	v_fma_f32 v237, -v65, v9, v237
	v_fma_f32 v238, -v66, v13, v238
	v_fma_f32 v239, -v67, v14, v239
	v_fma_f32 v236, -v68, v15, v236
	v_fma_f32 v237, -v69, v16, v237
	v_fma_f32 v238, -v70, v17, v238
	v_fma_f32 v239, -v71, v18, v239
	ds_read_b128 v[56:59], v240 offset:6256
	ds_read_b128 v[60:63], v240 offset:6272
	ds_read_b128 v[64:67], v240 offset:6288
	ds_read_b128 v[68:71], v240 offset:6304
	s_waitcnt lgkmcnt(4)
	v_fma_f32 v236, -v220, v19, v236
	v_fma_f32 v237, -v221, v20, v237
	v_fma_f32 v238, -v222, v21, v238
	v_fma_f32 v239, -v223, v22, v239
	v_fma_f32 v236, -v224, v23, v236
	v_fma_f32 v237, -v225, v24, v237
	v_add_f32_e32 v236, v236, v237
	v_add_f32_e32 v238, v238, v239
	v_add_f32_e32 v25, v236, v238
	ds_write_b32 v241, v25 offset:5632
	ds_read_b128 v[220:223], v240 offset:6320
	ds_read_b128 v[224:227], v240 offset:6336
	v_cmp_eq_u32_e32 vcc, 23, v178
	v_mov_b32_e32 v237, 0
	v_mov_b32_e32 v238, 0
	v_mov_b32_e32 v239, 0
	v_cndmask_b32_e64 v236, 0, 1.0, vcc
	s_waitcnt lgkmcnt(3)
	v_fma_f32 v236, -v56, v0, v236
	v_fma_f32 v237, -v57, v1, v237
	v_fma_f32 v238, -v58, v2, v238
	v_fma_f32 v239, -v59, v3, v239
	v_fma_f32 v236, -v60, v4, v236
	v_fma_f32 v237, -v61, v5, v237
	v_fma_f32 v238, -v62, v6, v238
	v_fma_f32 v239, -v63, v7, v239
	v_fma_f32 v236, -v64, v8, v236
	v_fma_f32 v237, -v65, v9, v237
	v_fma_f32 v238, -v66, v13, v238
	v_fma_f32 v239, -v67, v14, v239
	v_fma_f32 v236, -v68, v15, v236
	v_fma_f32 v237, -v69, v16, v237
	v_fma_f32 v238, -v70, v17, v238
	v_fma_f32 v239, -v71, v18, v239
	ds_read_b128 v[56:59], v240 offset:6528
	ds_read_b128 v[60:63], v240 offset:6544
	ds_read_b128 v[64:67], v240 offset:6560
	ds_read_b128 v[68:71], v240 offset:6576
	s_waitcnt lgkmcnt(4)
	v_fma_f32 v236, -v220, v19, v236
	v_fma_f32 v237, -v221, v20, v237
	v_fma_f32 v238, -v222, v21, v238
	v_fma_f32 v239, -v223, v22, v239
	v_fma_f32 v236, -v224, v23, v236
	v_fma_f32 v237, -v225, v24, v237
	v_fma_f32 v238, -v226, v25, v238
	v_add_f32_e32 v236, v236, v237
	v_add_f32_e32 v238, v238, v239
	v_add_f32_e32 v31, v236, v238
	ds_write_b32 v241, v31 offset:5888
	ds_read_b128 v[220:223], v240 offset:6592
	ds_read_b128 v[224:227], v240 offset:6608
	v_cmp_eq_u32_e32 vcc, 24, v178
	v_mov_b32_e32 v237, 0
	v_mov_b32_e32 v238, 0
	v_mov_b32_e32 v239, 0
	v_cndmask_b32_e64 v236, 0, 1.0, vcc
	s_waitcnt lgkmcnt(3)
	v_fma_f32 v236, -v56, v0, v236
	v_fma_f32 v237, -v57, v1, v237
	v_fma_f32 v238, -v58, v2, v238
	v_fma_f32 v239, -v59, v3, v239
	v_fma_f32 v236, -v60, v4, v236
	v_fma_f32 v237, -v61, v5, v237
	v_fma_f32 v238, -v62, v6, v238
	v_fma_f32 v239, -v63, v7, v239
	v_fma_f32 v236, -v64, v8, v236
	v_fma_f32 v237, -v65, v9, v237
	v_fma_f32 v238, -v66, v13, v238
	v_fma_f32 v239, -v67, v14, v239
	v_fma_f32 v236, -v68, v15, v236
	v_fma_f32 v237, -v69, v16, v237
	v_fma_f32 v238, -v70, v17, v238
	v_fma_f32 v239, -v71, v18, v239
	ds_read_b128 v[56:59], v240 offset:6800
	ds_read_b128 v[60:63], v240 offset:6816
	ds_read_b128 v[64:67], v240 offset:6832
	ds_read_b128 v[68:71], v240 offset:6848
	s_waitcnt lgkmcnt(4)
	v_fma_f32 v236, -v220, v19, v236
	v_fma_f32 v237, -v221, v20, v237
	v_fma_f32 v238, -v222, v21, v238
	v_fma_f32 v239, -v223, v22, v239
	v_fma_f32 v236, -v224, v23, v236
	v_fma_f32 v237, -v225, v24, v237
	v_fma_f32 v238, -v226, v25, v238
	v_fma_f32 v239, -v227, v31, v239
	v_add_f32_e32 v236, v236, v237
	v_add_f32_e32 v238, v238, v239
	v_add_f32_e32 v38, v236, v238
	ds_write_b32 v241, v38 offset:6144
	ds_read_b128 v[220:223], v240 offset:6864
	ds_read_b128 v[224:227], v240 offset:6880
	ds_read_b128 v[228:231], v240 offset:6896
	v_cmp_eq_u32_e32 vcc, 25, v178
	v_mov_b32_e32 v237, 0
	v_mov_b32_e32 v238, 0
	v_mov_b32_e32 v239, 0
	v_cndmask_b32_e64 v236, 0, 1.0, vcc
	s_waitcnt lgkmcnt(4)
	v_fma_f32 v236, -v56, v0, v236
	v_fma_f32 v237, -v57, v1, v237
	v_fma_f32 v238, -v58, v2, v238
	v_fma_f32 v239, -v59, v3, v239
	v_fma_f32 v236, -v60, v4, v236
	v_fma_f32 v237, -v61, v5, v237
	v_fma_f32 v238, -v62, v6, v238
	v_fma_f32 v239, -v63, v7, v239
	v_fma_f32 v236, -v64, v8, v236
	v_fma_f32 v237, -v65, v9, v237
	v_fma_f32 v238, -v66, v13, v238
	v_fma_f32 v239, -v67, v14, v239
	v_fma_f32 v236, -v68, v15, v236
	v_fma_f32 v237, -v69, v16, v237
	v_fma_f32 v238, -v70, v17, v238
	v_fma_f32 v239, -v71, v18, v239
	ds_read_b128 v[56:59], v240 offset:7072
	ds_read_b128 v[60:63], v240 offset:7088
	ds_read_b128 v[64:67], v240 offset:7104
	ds_read_b128 v[68:71], v240 offset:7120
	s_waitcnt lgkmcnt(4)
	v_fma_f32 v236, -v220, v19, v236
	v_fma_f32 v237, -v221, v20, v237
	v_fma_f32 v238, -v222, v21, v238
	v_fma_f32 v239, -v223, v22, v239
	v_fma_f32 v236, -v224, v23, v236
	v_fma_f32 v237, -v225, v24, v237
	v_fma_f32 v238, -v226, v25, v238
	v_fma_f32 v239, -v227, v31, v239
	v_fma_f32 v236, -v228, v38, v236
	v_add_f32_e32 v236, v236, v237
	v_add_f32_e32 v238, v238, v239
	v_add_f32_e32 v39, v236, v238
	ds_write_b32 v241, v39 offset:6400
	ds_read_b128 v[220:223], v240 offset:7136
	ds_read_b128 v[224:227], v240 offset:7152
	ds_read_b128 v[228:231], v240 offset:7168
	v_cmp_eq_u32_e32 vcc, 26, v178
	v_mov_b32_e32 v237, 0
	v_mov_b32_e32 v238, 0
	v_mov_b32_e32 v239, 0
	v_cndmask_b32_e64 v236, 0, 1.0, vcc
	s_waitcnt lgkmcnt(4)
; DI void gdn_prep_unit(const Params& p, int U, char* lds) {
;     ...
;     if (wid < 2 && lane < 32) {
;       const int o = 32 * wid;
;       for (int i = 0; i < 32; ++i) {
;         float a0 = (lane == i) ? 1.f : 0.f, a1 = 0.f, a2 = 0.f, a3 = 0.f;
;         const float* Li = Lm + (o + i) * 68 + o;
;         int j = 0;
; #pragma unroll 4
;         for (; j + 4 <= i; j += 4) {
;           const f32x4 Lv = *(const f32x4*)(Li + j);
;           a0 -= Lv[0] * Ts[(o + j) * 64 + o + lane]; a1 -= Lv[1] * Ts[(o + j + 1) * 64 + o + lane]; a2 -= Lv[2] * Ts[(o + j + 2) * 64 + o + lane]; a3 -= Lv[3] * Ts[(o + j + 3) * 64 + o + lane];
;         }
;         for (; j < i; ++j) a0 -= Li[j] * Ts[(o + j) * 64 + o + lane];
;         Ts[(o + i) * 64 + o + lane] = (a0 + a1) + (a2 + a3);
	v_fma_f32 v236, -v56, v0, v236
	v_fma_f32 v237, -v57, v1, v237
	v_fma_f32 v238, -v58, v2, v238
	v_fma_f32 v239, -v59, v3, v239
	v_fma_f32 v236, -v60, v4, v236
	v_fma_f32 v237, -v61, v5, v237
	v_fma_f32 v238, -v62, v6, v238
	v_fma_f32 v239, -v63, v7, v239
	v_fma_f32 v236, -v64, v8, v236
	v_fma_f32 v237, -v65, v9, v237
	v_fma_f32 v238, -v66, v13, v238
	v_fma_f32 v239, -v67, v14, v239
	v_fma_f32 v236, -v68, v15, v236
	v_fma_f32 v237, -v69, v16, v237
	v_fma_f32 v238, -v70, v17, v238
	v_fma_f32 v239, -v71, v18, v239
	ds_read_b128 v[56:59], v240 offset:7344
	ds_read_b128 v[60:63], v240 offset:7360
	ds_read_b128 v[64:67], v240 offset:7376
	ds_read_b128 v[68:71], v240 offset:7392
	s_waitcnt lgkmcnt(4)
	v_fma_f32 v236, -v220, v19, v236
	v_fma_f32 v237, -v221, v20, v237
	v_fma_f32 v238, -v222, v21, v238
	v_fma_f32 v239, -v223, v22, v239
	v_fma_f32 v236, -v224, v23, v236
	v_fma_f32 v237, -v225, v24, v237
	v_fma_f32 v238, -v226, v25, v238
	v_fma_f32 v239, -v227, v31, v239
	v_fma_f32 v236, -v228, v38, v236
	v_fma_f32 v237, -v229, v39, v237
	v_add_f32_e32 v236, v236, v237
	v_add_f32_e32 v238, v238, v239
	v_add_f32_e32 v44, v236, v238
	ds_write_b32 v241, v44 offset:6656
	ds_read_b128 v[220:223], v240 offset:7408
	ds_read_b128 v[224:227], v240 offset:7424
	ds_read_b128 v[228:231], v240 offset:7440
	v_cmp_eq_u32_e32 vcc, 27, v178
	v_mov_b32_e32 v237, 0
	v_mov_b32_e32 v238, 0
	v_mov_b32_e32 v239, 0
	v_cndmask_b32_e64 v236, 0, 1.0, vcc
	s_waitcnt lgkmcnt(4)
	v_fma_f32 v236, -v56, v0, v236
	v_fma_f32 v237, -v57, v1, v237
	v_fma_f32 v238, -v58, v2, v238
	v_fma_f32 v239, -v59, v3, v239
	v_fma_f32 v236, -v60, v4, v236
	v_fma_f32 v237, -v61, v5, v237
	v_fma_f32 v238, -v62, v6, v238
	v_fma_f32 v239, -v63, v7, v239
	v_fma_f32 v236, -v64, v8, v236
	v_fma_f32 v237, -v65, v9, v237
	v_fma_f32 v238, -v66, v13, v238
	v_fma_f32 v239, -v67, v14, v239
	v_fma_f32 v236, -v68, v15, v236
	v_fma_f32 v237, -v69, v16, v237
	v_fma_f32 v238, -v70, v17, v238
	v_fma_f32 v239, -v71, v18, v239
	ds_read_b128 v[56:59], v240 offset:7616
	ds_read_b128 v[60:63], v240 offset:7632
	ds_read_b128 v[64:67], v240 offset:7648
	ds_read_b128 v[68:71], v240 offset:7664
	s_waitcnt lgkmcnt(4)
	v_fma_f32 v236, -v220, v19, v236
	v_fma_f32 v237, -v221, v20, v237
	v_fma_f32 v238, -v222, v21, v238
	v_fma_f32 v239, -v223, v22, v239
	v_fma_f32 v236, -v224, v23, v236
	v_fma_f32 v237, -v225, v24, v237
	v_fma_f32 v238, -v226, v25, v238
	v_fma_f32 v239, -v227, v31, v239
	v_fma_f32 v236, -v228, v38, v236
	v_fma_f32 v237, -v229, v39, v237
	v_fma_f32 v238, -v230, v44, v238
	v_add_f32_e32 v236, v236, v237
	v_add_f32_e32 v238, v238, v239
	v_add_f32_e32 v45, v236, v238
	ds_write_b32 v241, v45 offset:6912
	ds_read_b128 v[220:223], v240 offset:7680
	ds_read_b128 v[224:227], v240 offset:7696
	ds_read_b128 v[228:231], v240 offset:7712
	v_cmp_eq_u32_e32 vcc, 28, v178
	v_mov_b32_e32 v237, 0
	v_mov_b32_e32 v238, 0
	v_mov_b32_e32 v239, 0
	v_cndmask_b32_e64 v236, 0, 1.0, vcc
	s_waitcnt lgkmcnt(4)
	v_fma_f32 v236, -v56, v0, v236
	v_fma_f32 v237, -v57, v1, v237
	v_fma_f32 v238, -v58, v2, v238
	v_fma_f32 v239, -v59, v3, v239
	v_fma_f32 v236, -v60, v4, v236
	v_fma_f32 v237, -v61, v5, v237
	v_fma_f32 v238, -v62, v6, v238
	v_fma_f32 v239, -v63, v7, v239
	v_fma_f32 v236, -v64, v8, v236
	v_fma_f32 v237, -v65, v9, v237
	v_fma_f32 v238, -v66, v13, v238
	v_fma_f32 v239, -v67, v14, v239
	v_fma_f32 v236, -v68, v15, v236
	v_fma_f32 v237, -v69, v16, v237
	v_fma_f32 v238, -v70, v17, v238
	v_fma_f32 v239, -v71, v18, v239
	ds_read_b128 v[56:59], v240 offset:7888
	ds_read_b128 v[60:63], v240 offset:7904
	ds_read_b128 v[64:67], v240 offset:7920
	ds_read_b128 v[68:71], v240 offset:7936
	s_waitcnt lgkmcnt(4)
	v_fma_f32 v236, -v220, v19, v236
	v_fma_f32 v237, -v221, v20, v237
	v_fma_f32 v238, -v222, v21, v238
	v_fma_f32 v239, -v223, v22, v239
	v_fma_f32 v236, -v224, v23, v236
	v_fma_f32 v237, -v225, v24, v237
	v_fma_f32 v238, -v226, v25, v238
	v_fma_f32 v239, -v227, v31, v239
	v_fma_f32 v236, -v228, v38, v236
	v_fma_f32 v237, -v229, v39, v237
	v_fma_f32 v238, -v230, v44, v238
	v_fma_f32 v239, -v231, v45, v239
	v_add_f32_e32 v236, v236, v237
	v_add_f32_e32 v238, v238, v239
	v_add_f32_e32 v52, v236, v238
	ds_write_b32 v241, v52 offset:7168
	ds_read_b128 v[220:223], v240 offset:7952
	ds_read_b128 v[224:227], v240 offset:7968
	ds_read_b128 v[228:231], v240 offset:7984
	ds_read_b128 v[232:235], v240 offset:8000
	v_cmp_eq_u32_e32 vcc, 29, v178
	v_mov_b32_e32 v237, 0
	v_mov_b32_e32 v238, 0
	v_mov_b32_e32 v239, 0
	v_cndmask_b32_e64 v236, 0, 1.0, vcc
	s_waitcnt lgkmcnt(5)
; DI void gdn_prep_unit(const Params& p, int U, char* lds) {
;     ...
;     if (wid < 2 && lane < 32) {
;       const int o = 32 * wid;
;       for (int i = 0; i < 32; ++i) {
;         float a0 = (lane == i) ? 1.f : 0.f, a1 = 0.f, a2 = 0.f, a3 = 0.f;
;         const float* Li = Lm + (o + i) * 68 + o;
;         int j = 0;
; #pragma unroll 4
;         for (; j + 4 <= i; j += 4) {
;           const f32x4 Lv = *(const f32x4*)(Li + j);
;           a0 -= Lv[0] * Ts[(o + j) * 64 + o + lane]; a1 -= Lv[1] * Ts[(o + j + 1) * 64 + o + lane]; a2 -= Lv[2] * Ts[(o + j + 2) * 64 + o + lane]; a3 -= Lv[3] * Ts[(o + j + 3) * 64 + o + lane];
;         }
;         for (; j < i; ++j) a0 -= Li[j] * Ts[(o + j) * 64 + o + lane];
;         Ts[(o + i) * 64 + o + lane] = (a0 + a1) + (a2 + a3);
;       }
;     }
	v_fma_f32 v236, -v56, v0, v236
	v_fma_f32 v237, -v57, v1, v237
	v_fma_f32 v238, -v58, v2, v238
	v_fma_f32 v239, -v59, v3, v239
	v_fma_f32 v236, -v60, v4, v236
	v_fma_f32 v237, -v61, v5, v237
	v_fma_f32 v238, -v62, v6, v238
	v_fma_f32 v239, -v63, v7, v239
	v_fma_f32 v236, -v64, v8, v236
	v_fma_f32 v237, -v65, v9, v237
	v_fma_f32 v238, -v66, v13, v238
	v_fma_f32 v239, -v67, v14, v239
	v_fma_f32 v236, -v68, v15, v236
	v_fma_f32 v237, -v69, v16, v237
	v_fma_f32 v238, -v70, v17, v238
	v_fma_f32 v239, -v71, v18, v239
	ds_read_b128 v[56:59], v240 offset:8160
	ds_read_b128 v[60:63], v240 offset:8176
	ds_read_b128 v[64:67], v240 offset:8192
	ds_read_b128 v[68:71], v240 offset:8208
	s_waitcnt lgkmcnt(4)
	v_fma_f32 v236, -v220, v19, v236
	v_fma_f32 v237, -v221, v20, v237
	v_fma_f32 v238, -v222, v21, v238
	v_fma_f32 v239, -v223, v22, v239
	v_fma_f32 v236, -v224, v23, v236
	v_fma_f32 v237, -v225, v24, v237
	v_fma_f32 v238, -v226, v25, v238
	v_fma_f32 v239, -v227, v31, v239
	v_fma_f32 v236, -v228, v38, v236
	v_fma_f32 v237, -v229, v39, v237
	v_fma_f32 v238, -v230, v44, v238
	v_fma_f32 v239, -v231, v45, v239
	v_fma_f32 v236, -v232, v52, v236
	v_add_f32_e32 v236, v236, v237
	v_add_f32_e32 v238, v238, v239
	v_add_f32_e32 v53, v236, v238
	ds_write_b32 v241, v53 offset:7424
	ds_read_b128 v[220:223], v240 offset:8224
	ds_read_b128 v[224:227], v240 offset:8240
	ds_read_b128 v[228:231], v240 offset:8256
	ds_read_b128 v[232:235], v240 offset:8272
	v_cmp_eq_u32_e32 vcc, 30, v178
	v_mov_b32_e32 v237, 0
	v_mov_b32_e32 v238, 0
	v_mov_b32_e32 v239, 0
	v_cndmask_b32_e64 v236, 0, 1.0, vcc
	s_waitcnt lgkmcnt(5)
	v_fma_f32 v236, -v56, v0, v236
	v_fma_f32 v237, -v57, v1, v237
	v_fma_f32 v238, -v58, v2, v238
	v_fma_f32 v239, -v59, v3, v239
	v_fma_f32 v236, -v60, v4, v236
	v_fma_f32 v237, -v61, v5, v237
	v_fma_f32 v238, -v62, v6, v238
	v_fma_f32 v239, -v63, v7, v239
	v_fma_f32 v236, -v64, v8, v236
	v_fma_f32 v237, -v65, v9, v237
	v_fma_f32 v238, -v66, v13, v238
	v_fma_f32 v239, -v67, v14, v239
	v_fma_f32 v236, -v68, v15, v236
	v_fma_f32 v237, -v69, v16, v237
	v_fma_f32 v238, -v70, v17, v238
	v_fma_f32 v239, -v71, v18, v239
	ds_read_b128 v[56:59], v240 offset:8432
	ds_read_b128 v[60:63], v240 offset:8448
	ds_read_b128 v[64:67], v240 offset:8464
	ds_read_b128 v[68:71], v240 offset:8480
	s_waitcnt lgkmcnt(4)
	v_fma_f32 v236, -v220, v19, v236
	v_fma_f32 v237, -v221, v20, v237
	v_fma_f32 v238, -v222, v21, v238
	v_fma_f32 v239, -v223, v22, v239
	v_fma_f32 v236, -v224, v23, v236
	v_fma_f32 v237, -v225, v24, v237
	v_fma_f32 v238, -v226, v25, v238
	v_fma_f32 v239, -v227, v31, v239
	v_fma_f32 v236, -v228, v38, v236
	v_fma_f32 v237, -v229, v39, v237
	v_fma_f32 v238, -v230, v44, v238
	v_fma_f32 v239, -v231, v45, v239
	v_fma_f32 v236, -v232, v52, v236
	v_fma_f32 v237, -v233, v53, v237
	v_add_f32_e32 v236, v236, v237
	v_add_f32_e32 v238, v238, v239
	v_add_f32_e32 v72, v236, v238
	ds_write_b32 v241, v72 offset:7680
	ds_read_b128 v[220:223], v240 offset:8496
	ds_read_b128 v[224:227], v240 offset:8512
	ds_read_b128 v[228:231], v240 offset:8528
	ds_read_b128 v[232:235], v240 offset:8544
	v_cmp_eq_u32_e32 vcc, 31, v178
	v_mov_b32_e32 v237, 0
	v_mov_b32_e32 v238, 0
	v_mov_b32_e32 v239, 0
	v_cndmask_b32_e64 v236, 0, 1.0, vcc
	s_waitcnt lgkmcnt(5)
	v_fma_f32 v236, -v56, v0, v236
	v_fma_f32 v237, -v57, v1, v237
	v_fma_f32 v238, -v58, v2, v238
	v_fma_f32 v239, -v59, v3, v239
	v_fma_f32 v236, -v60, v4, v236
	v_fma_f32 v237, -v61, v5, v237
	v_fma_f32 v238, -v62, v6, v238
	v_fma_f32 v239, -v63, v7, v239
	v_fma_f32 v236, -v64, v8, v236
	v_fma_f32 v237, -v65, v9, v237
	v_fma_f32 v238, -v66, v13, v238
	v_fma_f32 v239, -v67, v14, v239
	v_fma_f32 v236, -v68, v15, v236
	v_fma_f32 v237, -v69, v16, v237
	v_fma_f32 v238, -v70, v17, v238
	v_fma_f32 v239, -v71, v18, v239
	s_waitcnt lgkmcnt(0)
	v_fma_f32 v236, -v220, v19, v236
	v_fma_f32 v237, -v221, v20, v237
	v_fma_f32 v238, -v222, v21, v238
	v_fma_f32 v239, -v223, v22, v239
	v_fma_f32 v236, -v224, v23, v236
	v_fma_f32 v237, -v225, v24, v237
	v_fma_f32 v238, -v226, v25, v238
	v_fma_f32 v239, -v227, v31, v239
	v_fma_f32 v236, -v228, v38, v236
	v_fma_f32 v237, -v229, v39, v237
	v_fma_f32 v238, -v230, v44, v238
	v_fma_f32 v239, -v231, v45, v239
	v_fma_f32 v236, -v232, v52, v236
	v_fma_f32 v237, -v233, v53, v237
	v_fma_f32 v238, -v234, v72, v238
	v_add_f32_e32 v236, v236, v237
	v_add_f32_e32 v238, v238, v239
	v_add_f32_e32 v73, v236, v238
	ds_write_b32 v241, v73 offset:7936
